# scan compute waves: two independent packed FMAs hoisted above the denominator-permute wait (on the full stack)
# speedup vs baseline: 1.0048x; 1.0035x over previous
; #define LAS __attribute__((address_space(3)))
; __device__ __forceinline__ void p4_scan(const Args& a, const Frame& F) {
;     ...
;                 const float MtA = fmaxf(PML[trA], mcar), MtB = fmaxf(PML[trB], mcar);
;                 const float decA = __expf(mcar - MtA), emtA = __expf(-(BL[trA] + MtA)), decB = __expf(mcar - MtB), emtB = __expf(-(BL[trB] + MtB));
;     ...
;                     const float denA = __shfl(acc2A[2][0] + decA * acc3A[2][0], c), denB = __shfl(acc2B[2][0] + decB * acc3B[2][0], c);
;                     const float invA = frcp_(fmaxf(fabsf(denA), emtA)), invB = frcp_(fmaxf(fabsf(denB), emtB));
;                     { bf16* HXs = store ? HX : (bf16*)(a.ws + WS_H2) - (size_t)T * 512;
;                         const int lnh = c + 16 * q, pfh = (lnh >> 2) & 15, pqh = lnh & 3, bah = 4 * (pfh + 16 * pqh);
;                         const int tokA = base + (dir ? 127 - (16 * ta + pfh) : (16 * ta + pfh)), tokB = base + (dir ? 127 - (16 * tb + pfh) : (16 * tb + pfh));
; #pragma unroll
;                         for (int mt = 0; mt < 2; ++mt) { const f32x4 vA = (acc2A[mt] + acc3A[mt] * decA) * invA, vB = (acc2B[mt] + acc3B[mt] * decB) * invB;
;                             u32x2 o; o.x = pg8::cvt_pk_bf16(vA[0], vA[1]); o.y = pg8::cvt_pk_bf16(vA[2], vA[3]);
;                             o.x = (unsigned)__builtin_amdgcn_ds_bpermute(bah, (int)o.x); o.y = (unsigned)__builtin_amdgcn_ds_bpermute(bah, (int)o.y);
;                             *(u32x2*)(HXs + (size_t)tokA * 512 + h * 128 + vs * 32 + 16 * mt + 4 * pqh) = o;
;                             o.x = pg8::cvt_pk_bf16(vB[0], vB[1]); o.y = pg8::cvt_pk_bf16(vB[2], vB[3]);
;                             o.x = (unsigned)__builtin_amdgcn_ds_bpermute(bah, (int)o.x); o.y = (unsigned)__builtin_amdgcn_ds_bpermute(bah, (int)o.y);
;                             *(u32x2*)(HXs + (size_t)tokB * 512 + h * 128 + vs * 32 + 16 * mt + 4 * pqh) = o; } }
;                 }
;                 LDS_BARRIER();
;                 {
;                     bf16x8 vf[3][4];
; #pragma unroll
;                     for (int nt = 0; nt < 3; ++nt)
; #pragma unroll
;                         for (int ks = 0; ks < 4; ++ks) vf[nt][ks] = *(const LAS bf16x8*)(L + vacur + (16 * nt + c) * SP + (ks * 32 + q * 8) * 2);
; #pragma unroll
;                     for (int d2 = 0; d2 < 2; ++d2) {
;                         unsigned ka[8];
; #pragma unroll
.LBB0_449:
	v_max_f32_e32 v49, v153, v153
	v_max_f32_e32 v49, v49, v205
	v_sub_f32_e32 v50, v201, v49
	v_mul_f32_e32 v50, 0x3fb8aa3b, v50
	v_exp_f32_e32 v72, v50
	s_waitcnt lgkmcnt(1)
	v_add_f32_e32 v50, v204, v203
	v_add_f32_e32 v71, v152, v49
	v_sub_f32_e32 v49, v201, v204
	v_mul_f32_e32 v51, 0xbfb8aa3b, v50
	v_sub_f32_e32 v50, v201, v53
	v_mul_f32_e32 v49, 0x3fb8aa3b, v49
	v_mul_f32_e32 v73, 0x3fb8aa3b, v50
	s_waitcnt lgkmcnt(0)
	s_barrier
	v_add_f32_e32 v50, v53, v202
	v_mul_f32_e32 v53, 0xbfb8aa3b, v50
	v_exp_f32_e32 v50, v49
	v_exp_f32_e32 v76, v73
	v_exp_f32_e32 v49, v51
	v_exp_f32_e32 v51, v53
	v_fmac_f32_e32 v70, v52, v50
	ds_bpermute_b32 v52, v200, v70
	v_fmac_f32_e32 v74, v48, v76
	ds_bpermute_b32 v53, v200, v74
	v_pk_fma_f32 v[44:45], v[44:45], v[50:51], v[66:67] op_sel_hi:[1,0,1]
	v_pk_fma_f32 v[46:47], v[46:47], v[50:51], v[68:69] op_sel_hi:[1,0,1]
	s_and_b64 s[6:7], s[50:51], exec
	s_cselect_b32 s6, s92, 0x1de20
	s_waitcnt lgkmcnt(1)
	v_max_f32_e64 v48, |v52|, |v52|
	v_max_f32_e32 v48, v48, v49
	v_rcp_f32_e32 v48, v48
	s_waitcnt lgkmcnt(0)
	v_max_f32_e64 v49, |v53|, |v53|
	s_cmp_gt_u32 s11, 1
	v_max_f32_e32 v49, v49, v51
	s_cselect_b32 s8, s77, 0x23200000
	v_add_u32_e32 v74, s64, v186
	v_pk_mul_f32 v[44:45], v[44:45], v[48:49] op_sel_hi:[1,0]
	s_cselect_b32 s7, 0, 0
	s_add_u32 s8, s72, s8
	v_ashrrev_i32_e32 v75, 31, v74
	v_pk_mul_f32 v[46:47], v[46:47], v[48:49] op_sel_hi:[1,0]
	v_cvt_pk_bf16_f32 v44, v44, v45
	v_rcp_f32_e32 v52, v49
	v_cvt_pk_bf16_f32 v45, v46, v47
	s_addc_u32 s9, s73, s7
	v_lshlrev_b64 v[74:75], 10, v[74:75]
	ds_bpermute_b32 v44, v185, v44
	ds_bpermute_b32 v45, v185, v45
	v_lshl_add_u64 v[74:75], s[8:9], 0, v[74:75]
	v_lshl_add_u64 v[74:75], v[74:75], 0, s[44:45]
	s_mov_b32 s11, s45
	v_lshl_add_u64 v[74:75], v[74:75], 0, s[10:11]
	v_pk_fma_f32 v[40:41], v[40:41], v[76:77], v[62:63] op_sel_hi:[1,0,1]
	v_add_u32_e32 v78, s64, v187
	v_lshl_add_u64 v[74:75], v[74:75], 0, v[144:145]
	v_pk_fma_f32 v[42:43], v[42:43], v[76:77], v[64:65] op_sel_hi:[1,0,1]
	v_pk_mul_f32 v[40:41], v[40:41], v[52:53] op_sel_hi:[1,0]
	v_ashrrev_i32_e32 v79, 31, v78
	v_pk_mul_f32 v[42:43], v[42:43], v[52:53] op_sel_hi:[1,0]
	v_cvt_pk_bf16_f32 v40, v40, v41
	v_cvt_pk_bf16_f32 v41, v42, v43
	v_lshlrev_b64 v[78:79], 10, v[78:79]
	ds_bpermute_b32 v40, v185, v40
	ds_bpermute_b32 v41, v185, v41
	s_waitcnt lgkmcnt(2)
	global_store_dwordx2 v[74:75], v[44:45], off
	v_lshl_add_u64 v[78:79], s[8:9], 0, v[78:79]
	v_lshl_add_u64 v[78:79], v[78:79], 0, s[44:45]
	v_lshl_add_u64 v[78:79], v[78:79], 0, s[10:11]
	v_pk_fma_f32 v[36:37], v[36:37], v[50:51], v[58:59] op_sel_hi:[1,0,1]
	v_lshl_add_u64 v[78:79], v[78:79], 0, v[144:145]
	v_pk_fma_f32 v[38:39], v[38:39], v[50:51], v[60:61] op_sel_hi:[1,0,1]
	v_pk_mul_f32 v[36:37], v[36:37], v[48:49] op_sel_hi:[1,0]
	v_pk_mul_f32 v[38:39], v[38:39], v[48:49] op_sel_hi:[1,0]
	v_cvt_pk_bf16_f32 v36, v36, v37
	ds_bpermute_b32 v36, v185, v36
	v_cvt_pk_bf16_f32 v37, v38, v39
	ds_bpermute_b32 v37, v185, v37
	s_waitcnt lgkmcnt(2)
	global_store_dwordx2 v[78:79], v[40:41], off
	v_pk_fma_f32 v[32:33], v[32:33], v[76:77], v[54:55] op_sel_hi:[1,0,1]
	v_pk_fma_f32 v[34:35], v[34:35], v[76:77], v[56:57] op_sel_hi:[1,0,1]
	v_pk_mul_f32 v[32:33], v[32:33], v[52:53] op_sel_hi:[1,0]
	v_pk_mul_f32 v[34:35], v[34:35], v[52:53] op_sel_hi:[1,0]
	v_cvt_pk_bf16_f32 v32, v32, v33
	v_cvt_pk_bf16_f32 v33, v34, v35
	ds_bpermute_b32 v32, v185, v32
	ds_bpermute_b32 v33, v185, v33
	s_waitcnt lgkmcnt(2)
	global_store_dwordx2 v[74:75], v[36:37], off offset:32
	v_add_u32_e32 v36, s6, v189
	s_add_i32 s6, s35, 0
	v_add_u32_e32 v73, s6, v172
	v_pk_mul_f32 v[10:11], v[10:11], v[72:73] op_sel_hi:[1,0]
	s_waitcnt lgkmcnt(0)
	global_store_dwordx2 v[78:79], v[32:33], off offset:32
	s_waitcnt lgkmcnt(0)
	v_pk_mul_f32 v[8:9], v[8:9], v[72:73] op_sel_hi:[1,0]
	ds_read_b128 v[52:55], v36
	ds_read_b128 v[56:59], v36 offset:64
	ds_read_b128 v[44:47], v36 offset:128
	ds_read_b128 v[32:35], v36 offset:192
	ds_read_b128 v[60:63], v36 offset:4352
	ds_read_b128 v[64:67], v36 offset:4416
	ds_read_b128 v[48:51], v36 offset:4480
	ds_read_b128 v[40:43], v36 offset:4544
	ds_read_b128 v[74:77], v36 offset:8704
	ds_read_b128 v[78:81], v36 offset:8768
	ds_read_b128 v[82:85], v36 offset:8832
	ds_read_b128 v[36:39], v36 offset:8896
	v_add_u32_e32 v68, s6, v148
	v_add_u32_e32 v69, s6, v149
	v_add_u32_e32 v70, s6, v171
	v_add_u32_e32 v102, s6, v173
	v_add_u32_e32 v103, s6, v174
	v_add_u32_e32 v104, s6, v175
	v_add_u32_e32 v105, s6, v176
	ds_read_b64_tr_b16 v[98:99], v68
	ds_read_b64_tr_b16 v[100:101], v69
	ds_read_b64_tr_b16 v[94:95], v70
	ds_read_b64_tr_b16 v[96:97], v73
	ds_read_b64_tr_b16 v[90:91], v102
	ds_read_b64_tr_b16 v[92:93], v103
	ds_read_b64_tr_b16 v[86:87], v104
	ds_read_b64_tr_b16 v[88:89], v105
	s_waitcnt lgkmcnt(0)
	v_pk_mul_f32 v[14:15], v[14:15], v[72:73] op_sel_hi:[1,0]
	s_waitcnt lgkmcnt(11)
	v_mfma_f32_16x16x32_bf16 v[8:11], v[98:101], v[52:55], v[8:11]
	v_mul_f32_e64 v12, v12, v72
	v_mul_f32_e64 v13, v13, v72
	v_pk_mul_f32 v[18:19], v[18:19], v[72:73] op_sel_hi:[1,0]
	v_pk_mul_f32 v[16:17], v[16:17], v[72:73] op_sel_hi:[1,0]
	s_waitcnt lgkmcnt(10)
; #define LAS __attribute__((address_space(3)))
; __device__ __forceinline__ unsigned pk2(float lo, float hi) { return f2bf(lo) | (f2bf(hi) << 16); }
; #define LDS_BARRIER() do { asm volatile("s_waitcnt lgkmcnt(0)" ::: "memory"); __builtin_amdgcn_s_barrier(); asm volatile("" ::: "memory"); } while (0)
; __device__ __forceinline__ void p4_scan(const Args& a, const Frame& F) {
;     ...
;                         for (int i = 0; i < 8; ++i) ka[i] = Lb + (unsigned)kcur + kadA[i] + (d2 ? 32u : 0u);
;                         u32x2 kr[8]; tr_read_k8(kr, ka);
; #pragma unroll
;                         for (int nt = 0; nt < 3; ++nt) accC[d2][nt] = accC[d2][nt] * cd;
; #pragma unroll
;                         for (int ks = 0; ks < 4; ++ks) { const bf16x8 af = mk_frag(kr[ks * 2], kr[ks * 2 + 1]);
; #pragma unroll
;                             for (int nt = 0; nt < 3; ++nt) accC[d2][nt] = __builtin_amdgcn_mfma_f32_16x16x32_bf16(af, vf[nt][ks], accC[d2][nt], 0, 0, 0); }
; #pragma unroll
;                         for (int nt = 0; nt < 3; ++nt) { u32x2 o; o.x = pk2(accC[d2][nt][0], accC[d2][nt][1]); o.y = pk2(accC[d2][nt][2], accC[d2][nt][3]);
;                             *(LAS u32x2*)(L + S_CT + (16 * nt + c) * SP + (16 * (2 * w + d2) + 4 * q) * 2) = o; }
;                     }
;                 }
;                 mcar = mnew;
;                 btot = pbt; pmx = ppx;
;                 LDS_BARRIER();
	v_mfma_f32_16x16x32_bf16 v[8:11], v[94:97], v[56:59], v[8:11]
	s_add_i32 s6, s6, 32
	v_add_u32_e32 v73, s6, v172
	v_pk_mul_f32 v[22:23], v[22:23], v[72:73] op_sel_hi:[1,0]
	s_waitcnt lgkmcnt(7)
	v_mfma_f32_16x16x32_bf16 v[12:15], v[98:101], v[60:63], v[12:15]
	v_mul_f32_e64 v20, v20, v72
	v_mul_f32_e64 v21, v21, v72
	v_add_u32_e32 v102, s6, v173
	v_add_u32_e32 v103, s6, v174
	v_mfma_f32_16x16x32_bf16 v[8:11], v[90:93], v[44:47], v[8:11]
	v_add_u32_e32 v104, s6, v175
	v_add_u32_e32 v105, s6, v176
	v_pk_mul_f32 v[26:27], v[26:27], v[72:73] op_sel_hi:[1,0]
	s_waitcnt lgkmcnt(6)
	v_mfma_f32_16x16x32_bf16 v[12:15], v[94:97], v[64:67], v[12:15]
	v_mul_f32_e64 v24, v24, v72
	v_mul_f32_e64 v25, v25, v72
	v_pk_mul_f32 v[30:31], v[30:31], v[72:73] op_sel_hi:[1,0]
	v_pk_mul_f32 v[28:29], v[28:29], v[72:73] op_sel_hi:[1,0]
	v_mfma_f32_16x16x32_bf16 v[8:11], v[86:89], v[32:35], v[8:11]
	s_cmpk_eq_i32 s34, 0x42
	v_mov_b32_e32 v201, v71
	s_mov_b32 s11, s34
	s_waitcnt lgkmcnt(3)
	v_mfma_f32_16x16x32_bf16 v[16:19], v[98:101], v[74:77], v[16:19]
	s_nop 1
	s_nop 0
	v_bfe_u32 v68, v8, 16, 1
	v_add3_u32 v68, v8, v68, s93
	v_mfma_f32_16x16x32_bf16 v[12:15], v[90:93], v[48:51], v[12:15]
	v_bfe_u32 v69, v9, 16, 1
	v_lshrrev_b32_e32 v68, 16, v68
	v_add3_u32 v69, v9, v69, s93
	s_waitcnt lgkmcnt(2)
	v_mfma_f32_16x16x32_bf16 v[16:19], v[94:97], v[78:81], v[16:19]
	v_and_or_b32 v68, v69, s94, v68
	v_bfe_u32 v69, v10, 16, 1
	v_add3_u32 v69, v10, v69, s93
	v_mfma_f32_16x16x32_bf16 v[12:15], v[86:89], v[40:43], v[12:15]
	v_bfe_u32 v70, v11, 16, 1
	v_lshrrev_b32_e32 v69, 16, v69
	v_add3_u32 v70, v11, v70, s93
	s_waitcnt lgkmcnt(1)
	v_mfma_f32_16x16x32_bf16 v[16:19], v[90:93], v[82:85], v[16:19]
	v_and_or_b32 v69, v70, s94, v69
	ds_write_b64 v197, v[68:69]
	s_nop 0
	v_bfe_u32 v68, v12, 16, 1
	v_add3_u32 v68, v12, v68, s93
	v_bfe_u32 v69, v13, 16, 1
	v_lshrrev_b32_e32 v68, 16, v68
	v_add3_u32 v69, v13, v69, s93
	s_waitcnt lgkmcnt(1)
	v_mfma_f32_16x16x32_bf16 v[16:19], v[86:89], v[36:39], v[16:19]
	v_and_or_b32 v68, v69, s94, v68
	v_bfe_u32 v69, v14, 16, 1
	v_add3_u32 v69, v14, v69, s93
	v_bfe_u32 v70, v15, 16, 1
	v_lshrrev_b32_e32 v69, 16, v69
	v_add3_u32 v70, v15, v70, s93
	v_and_or_b32 v69, v70, s94, v69
	ds_write_b64 v197, v[68:69] offset:4352
	v_bfe_u32 v68, v16, 16, 1
	v_add3_u32 v68, v16, v68, s93
	v_bfe_u32 v69, v17, 16, 1
	v_lshrrev_b32_e32 v68, 16, v68
	v_add3_u32 v69, v17, v69, s93
	v_and_or_b32 v68, v69, s94, v68
	v_bfe_u32 v69, v18, 16, 1
	v_add3_u32 v69, v18, v69, s93
	v_bfe_u32 v70, v19, 16, 1
	v_lshrrev_b32_e32 v69, 16, v69
	v_add3_u32 v70, v19, v70, s93
	v_and_or_b32 v69, v70, s94, v69
	ds_write_b64 v197, v[68:69] offset:8704
	v_add_u32_e32 v68, s6, v148
	v_add_u32_e32 v69, s6, v149
	v_add_u32_e32 v70, s6, v171
	ds_read_b64_tr_b16 v[98:99], v68
	ds_read_b64_tr_b16 v[100:101], v69
	ds_read_b64_tr_b16 v[94:95], v70
	ds_read_b64_tr_b16 v[96:97], v73
	ds_read_b64_tr_b16 v[90:91], v102
	ds_read_b64_tr_b16 v[92:93], v103
	ds_read_b64_tr_b16 v[86:87], v104
	ds_read_b64_tr_b16 v[88:89], v105
	s_waitcnt lgkmcnt(0)
	s_nop 0
	v_mfma_f32_16x16x32_bf16 v[20:23], v[98:101], v[52:55], v[20:23]
	v_mfma_f32_16x16x32_bf16 v[20:23], v[94:97], v[56:59], v[20:23]
	v_mfma_f32_16x16x32_bf16 v[24:27], v[98:101], v[60:63], v[24:27]
	v_mfma_f32_16x16x32_bf16 v[20:23], v[90:93], v[44:47], v[20:23]
	v_mfma_f32_16x16x32_bf16 v[24:27], v[94:97], v[64:67], v[24:27]
	v_mfma_f32_16x16x32_bf16 v[20:23], v[86:89], v[32:35], v[20:23]
	v_mfma_f32_16x16x32_bf16 v[28:31], v[98:101], v[74:77], v[28:31]
	v_mfma_f32_16x16x32_bf16 v[24:27], v[90:93], v[48:51], v[24:27]
	s_nop 5
	v_bfe_u32 v32, v20, 16, 1
	v_add3_u32 v32, v20, v32, s93
	v_bfe_u32 v33, v21, 16, 1
	v_mfma_f32_16x16x32_bf16 v[28:31], v[94:97], v[78:81], v[28:31]
	v_lshrrev_b32_e32 v32, 16, v32
	v_add3_u32 v33, v21, v33, s93
	v_and_or_b32 v32, v33, s94, v32
	v_mfma_f32_16x16x32_bf16 v[24:27], v[86:89], v[40:43], v[24:27]
	v_bfe_u32 v33, v22, 16, 1
	v_add3_u32 v33, v22, v33, s93
	v_bfe_u32 v34, v23, 16, 1
	v_lshrrev_b32_e32 v33, 16, v33
	v_add3_u32 v34, v23, v34, s93
	v_mfma_f32_16x16x32_bf16 v[28:31], v[90:93], v[82:85], v[28:31]
	v_and_or_b32 v33, v34, s94, v33
	ds_write_b64 v197, v[32:33] offset:32
	v_bfe_u32 v32, v24, 16, 1
	v_add3_u32 v32, v24, v32, s93
	v_bfe_u32 v33, v25, 16, 1
	v_lshrrev_b32_e32 v32, 16, v32
	v_add3_u32 v33, v25, v33, s93
	v_mfma_f32_16x16x32_bf16 v[28:31], v[86:89], v[36:39], v[28:31]
	v_and_or_b32 v32, v33, s94, v32
	v_bfe_u32 v33, v26, 16, 1
	v_add3_u32 v33, v26, v33, s93
	v_bfe_u32 v34, v27, 16, 1
	v_lshrrev_b32_e32 v33, 16, v33
	v_add3_u32 v34, v27, v34, s93
	v_and_or_b32 v33, v34, s94, v33
	ds_write_b64 v197, v[32:33] offset:4384
	v_bfe_u32 v32, v28, 16, 1
	v_add3_u32 v32, v28, v32, s93
	v_bfe_u32 v33, v29, 16, 1
	v_lshrrev_b32_e32 v32, 16, v32
	v_add3_u32 v33, v29, v33, s93
	v_and_or_b32 v32, v33, s94, v32
	v_bfe_u32 v33, v30, 16, 1
	v_add3_u32 v33, v30, v33, s93
	v_bfe_u32 v34, v31, 16, 1
	v_lshrrev_b32_e32 v33, 16, v33
	v_add3_u32 v34, v31, v34, s93
	v_and_or_b32 v33, v34, s94, v33
	ds_write_b64 v197, v[32:33] offset:8736
	s_waitcnt lgkmcnt(0)
	s_barrier
	s_cbranch_scc1 .LBB0_472
